# speedup vs baseline: 1.0024x; 1.0002x over previous
_Z7gemm128ILi1ELi96EEv8GemmArgs:
	s_cmp_ge_u32 s2, 0x100
	s_cbranch_scc1 .Lou_exit
	s_load_dwordx4 s[4:7], s[0:1], 0x0
	s_load_dwordx2 s[8:9], s[0:1], 0x20
	s_load_dwordx2 s[10:11], s[0:1], 0x38
	s_load_dwordx2 s[24:25], s[0:1], 0x28
	s_load_dwordx2 s[26:27], s[0:1], 0x40
	s_load_dwordx2 s[28:29], s[0:1], 0x48
	s_and_b32 s12, s2, 7
	s_lshr_b32 s13, s2, 3
	s_lshl_b32 s12, s12, 5
	s_add_u32 s12, s12, s13
	s_and_b32 s13, s12, 3
	s_lshl_b32 s30, s13, 2
	s_lshr_b32 s12, s12, 2
	s_lshl_b32 s12, s12, 7
	s_mul_i32 s13, s13, 0xc0
	v_lshrrev_b32_e32 v1, 6, v0
	v_and_b32_e32 v14, 7, v0
	v_bfe_u32 v15, v0, 4, 3
	v_xor_b32_e32 v14, v14, v15
	v_readfirstlane_b32 s14, v1
	v_lshrrev_b32_e32 v15, 3, v0
	v_mul_u32_u24_e32 v15, 0x600, v15
	v_lshl_add_u32 v2, v14, 4, v15
	s_mov_b32 s22, 0xc000
	v_add_u32_e32 v3, s22, v2
	v_add_u32_e32 v4, s22, v3
	v_add_u32_e32 v5, s22, v4
	v_add_u32_e32 v6, s22, v5
	v_add_u32_e32 v7, s22, v6
	v_and_b32_e32 v14, 15, v0
	v_bfe_u32 v15, v0, 4, 2
	v_lshrrev_b32_e32 v16, 1, v14
	v_xor_b32_e32 v16, v16, v15
	v_lshlrev_b32_e32 v16, 4, v16
	v_bfe_u32 v17, v0, 7, 1
	v_bfe_u32 v18, v0, 6, 1
	v_lshl_add_u32 v19, v17, 6, v14
	v_lshl_add_u32 v8, v19, 7, v16
	v_mul_u32_u24_e32 v19, 0x60, v18
	v_add_u32_e32 v19, v19, v14
	v_lshl_add_u32 v9, v19, 7, v16
	v_add_u32_e32 v9, 0x4000, v9
	v_lshl_add_u32 v19, v17, 6, v14
	v_add_u32_e32 v19, s12, v19
	v_mul_u32_u24_e32 v19, 0xc00, v19
	v_mul_u32_u24_e32 v60, 0x60, v18
	v_lshl_add_u32 v60, v15, 2, v60
	v_add_u32_e32 v60, s13, v60
	v_lshl_add_u32 v56, v60, 2, v19
	s_mov_b32 s22, 0xc000
	v_add_u32_e32 v57, s22, v56
	v_add_u32_e32 v58, s22, v57
	v_add_u32_e32 v59, s22, v58
	v_mul_u32_u24_e32 v61, 0x60, v18
	v_lshl_add_u32 v61, v15, 2, v61
	v_add_u32_e32 v61, s13, v61
	v_lshlrev_b32_e32 v60, 2, v61
	s_waitcnt lgkmcnt(0)
	s_mul_i32 s22, s12, 0x600
	s_add_u32 s16, s4, s22
	s_addc_u32 s17, s5, 0
	s_mul_i32 s22, s13, 0x600
	s_add_u32 s18, s6, s22
	s_addc_u32 s19, s7, 0
	s_lshl_b32 s20, s14, 10
	s_mov_b32 s21, 0
	s_add_u32 m0, s20, 0x0
	s_nop 0
	global_load_lds_dwordx4 v2, s[16:17]
	s_add_u32 m0, s20, 0x1000
	s_nop 0
	global_load_lds_dwordx4 v3, s[16:17]
	s_add_u32 m0, s20, 0x2000
	s_nop 0
	global_load_lds_dwordx4 v4, s[16:17]
	s_add_u32 m0, s20, 0x3000
	s_nop 0
	global_load_lds_dwordx4 v5, s[16:17]
	s_add_u32 m0, s20, 0x4000
	s_nop 0
	global_load_lds_dwordx4 v2, s[18:19]
	s_add_u32 m0, s20, 0x5000
	s_nop 0
	global_load_lds_dwordx4 v3, s[18:19]
	s_add_u32 m0, s20, 0x6000
	s_nop 0
	global_load_lds_dwordx4 v4, s[18:19]
	s_add_u32 m0, s20, 0x7000
	s_nop 0
	global_load_lds_dwordx4 v5, s[18:19]
	s_add_u32 m0, s20, 0x8000
	s_nop 0
	global_load_lds_dwordx4 v6, s[18:19]
	s_add_u32 m0, s20, 0x9000
	s_nop 0
	global_load_lds_dwordx4 v7, s[18:19]
	s_add_u32 s16, s16, 0x80
	s_addc_u32 s17, s17, 0
	s_add_u32 s18, s18, 0x80
	s_addc_u32 s19, s19, 0
	s_add_u32 s20, s20, 0xa000
	s_sub_u32 s22, s20, 0x28000
	s_cmp_ge_u32 s20, 0x28000
	s_cselect_b32 s20, s22, s20
	s_add_u32 m0, s20, 0x0
	s_nop 0
	global_load_lds_dwordx4 v2, s[16:17]
	s_add_u32 m0, s20, 0x1000
	s_nop 0
	global_load_lds_dwordx4 v3, s[16:17]
	s_add_u32 m0, s20, 0x2000
	s_nop 0
	global_load_lds_dwordx4 v4, s[16:17]
	s_add_u32 m0, s20, 0x3000
	s_nop 0
	global_load_lds_dwordx4 v5, s[16:17]
	s_add_u32 m0, s20, 0x4000
	s_nop 0
	global_load_lds_dwordx4 v2, s[18:19]
	s_add_u32 m0, s20, 0x5000
	s_nop 0
	global_load_lds_dwordx4 v3, s[18:19]
	s_add_u32 m0, s20, 0x6000
	s_nop 0
	global_load_lds_dwordx4 v4, s[18:19]
	s_add_u32 m0, s20, 0x7000
	s_nop 0
	global_load_lds_dwordx4 v5, s[18:19]
	s_add_u32 m0, s20, 0x8000
	s_nop 0
	global_load_lds_dwordx4 v6, s[18:19]
	s_add_u32 m0, s20, 0x9000
	s_nop 0
	global_load_lds_dwordx4 v7, s[18:19]
	s_add_u32 s16, s16, 0x80
	s_addc_u32 s17, s17, 0
	s_add_u32 s18, s18, 0x80
	s_addc_u32 s19, s19, 0
	s_add_u32 s20, s20, 0xa000
	s_sub_u32 s22, s20, 0x28000
	s_cmp_ge_u32 s20, 0x28000
	s_cselect_b32 s20, s22, s20
	s_add_u32 m0, s20, 0x0
	s_nop 0
	global_load_lds_dwordx4 v2, s[16:17]
	s_add_u32 m0, s20, 0x1000
	s_nop 0
	global_load_lds_dwordx4 v3, s[16:17]
	s_add_u32 m0, s20, 0x2000
	s_nop 0
	global_load_lds_dwordx4 v4, s[16:17]
	s_add_u32 m0, s20, 0x3000
	s_nop 0
	global_load_lds_dwordx4 v5, s[16:17]
	s_add_u32 m0, s20, 0x4000
	s_nop 0
	global_load_lds_dwordx4 v2, s[18:19]
	s_add_u32 m0, s20, 0x5000
	s_nop 0
	global_load_lds_dwordx4 v3, s[18:19]
	s_add_u32 m0, s20, 0x6000
	s_nop 0
	global_load_lds_dwordx4 v4, s[18:19]
	s_add_u32 m0, s20, 0x7000
	s_nop 0
	global_load_lds_dwordx4 v5, s[18:19]
	s_add_u32 m0, s20, 0x8000
	s_nop 0
	global_load_lds_dwordx4 v6, s[18:19]
	s_add_u32 m0, s20, 0x9000
	s_nop 0
	global_load_lds_dwordx4 v7, s[18:19]
	s_add_u32 s16, s16, 0x80
	s_addc_u32 s17, s17, 0
	s_add_u32 s18, s18, 0x80
	s_addc_u32 s19, s19, 0
	s_add_u32 s20, s20, 0xa000
	s_sub_u32 s22, s20, 0x28000
	s_cmp_ge_u32 s20, 0x28000
	s_cselect_b32 s20, s22, s20
	s_add_u32 m0, s20, 0x0
	s_nop 0
	global_load_lds_dwordx4 v2, s[16:17]
	s_add_u32 m0, s20, 0x1000
	s_nop 0
	global_load_lds_dwordx4 v3, s[16:17]
	s_add_u32 m0, s20, 0x2000
	s_nop 0
	global_load_lds_dwordx4 v4, s[16:17]
	s_add_u32 m0, s20, 0x3000
	s_nop 0
	global_load_lds_dwordx4 v5, s[16:17]
	s_add_u32 m0, s20, 0x4000
	s_nop 0
	global_load_lds_dwordx4 v2, s[18:19]
	v_mov_b32_e32 v64, 0
	v_mov_b32_e32 v65, 0
	v_mov_b32_e32 v66, 0
	v_mov_b32_e32 v67, 0
	v_mov_b32_e32 v68, 0
	v_mov_b32_e32 v69, 0
	v_mov_b32_e32 v70, 0
	v_mov_b32_e32 v71, 0
	v_mov_b32_e32 v72, 0
	v_mov_b32_e32 v73, 0
	v_mov_b32_e32 v74, 0
	v_mov_b32_e32 v75, 0
	v_mov_b32_e32 v76, 0
	v_mov_b32_e32 v77, 0
	v_mov_b32_e32 v78, 0
	v_mov_b32_e32 v79, 0
	v_mov_b32_e32 v80, 0
	v_mov_b32_e32 v81, 0
	v_mov_b32_e32 v82, 0
	v_mov_b32_e32 v83, 0
	v_mov_b32_e32 v84, 0
	v_mov_b32_e32 v85, 0
	v_mov_b32_e32 v86, 0
	v_mov_b32_e32 v87, 0
	v_mov_b32_e32 v88, 0
	v_mov_b32_e32 v89, 0
	v_mov_b32_e32 v90, 0
	v_mov_b32_e32 v91, 0
	v_mov_b32_e32 v92, 0
	v_mov_b32_e32 v93, 0
	v_mov_b32_e32 v94, 0
	v_mov_b32_e32 v95, 0
	v_mov_b32_e32 v96, 0
	v_mov_b32_e32 v97, 0
	v_mov_b32_e32 v98, 0
	v_mov_b32_e32 v99, 0
	v_mov_b32_e32 v100, 0
	v_mov_b32_e32 v101, 0
	v_mov_b32_e32 v102, 0
	v_mov_b32_e32 v103, 0
	v_mov_b32_e32 v104, 0
	v_mov_b32_e32 v105, 0
	v_mov_b32_e32 v106, 0
	v_mov_b32_e32 v107, 0
	v_mov_b32_e32 v108, 0
	v_mov_b32_e32 v109, 0
	v_mov_b32_e32 v110, 0
	v_mov_b32_e32 v111, 0
	v_mov_b32_e32 v112, 0
	v_mov_b32_e32 v113, 0
	v_mov_b32_e32 v114, 0
	v_mov_b32_e32 v115, 0
	v_mov_b32_e32 v116, 0
	v_mov_b32_e32 v117, 0
	v_mov_b32_e32 v118, 0
	v_mov_b32_e32 v119, 0
	v_mov_b32_e32 v120, 0
	v_mov_b32_e32 v121, 0
	v_mov_b32_e32 v122, 0
	v_mov_b32_e32 v123, 0
	v_mov_b32_e32 v124, 0
	v_mov_b32_e32 v125, 0
	v_mov_b32_e32 v126, 0
	v_mov_b32_e32 v127, 0
	v_mov_b32_e32 v128, 0
	v_mov_b32_e32 v129, 0
	v_mov_b32_e32 v130, 0
	v_mov_b32_e32 v131, 0
	v_mov_b32_e32 v132, 0
	v_mov_b32_e32 v133, 0
	v_mov_b32_e32 v134, 0
	v_mov_b32_e32 v135, 0
	v_mov_b32_e32 v136, 0
	v_mov_b32_e32 v137, 0
	v_mov_b32_e32 v138, 0
	v_mov_b32_e32 v139, 0
	v_mov_b32_e32 v140, 0
	v_mov_b32_e32 v141, 0
	v_mov_b32_e32 v142, 0
	v_mov_b32_e32 v143, 0
	v_mov_b32_e32 v144, 0
	v_mov_b32_e32 v145, 0
	v_mov_b32_e32 v146, 0
	v_mov_b32_e32 v147, 0
	v_mov_b32_e32 v148, 0
	v_mov_b32_e32 v149, 0
	v_mov_b32_e32 v150, 0
	v_mov_b32_e32 v151, 0
	v_mov_b32_e32 v152, 0
	v_mov_b32_e32 v153, 0
	v_mov_b32_e32 v154, 0
	v_mov_b32_e32 v155, 0
	v_mov_b32_e32 v156, 0
	v_mov_b32_e32 v157, 0
	v_mov_b32_e32 v158, 0
	v_mov_b32_e32 v159, 0
	s_waitcnt vmcnt(25)
	s_barrier
	v_add_u32_e32 v10, s21, v8
	v_add_u32_e32 v12, s21, v9
	v_xor_b32_e32 v11, 64, v10
	v_xor_b32_e32 v13, 64, v12
	s_add_u32 s21, s21, 0xa000
	s_sub_u32 s23, s21, 0x28000
	s_cmp_ge_u32 s21, 0x28000
	s_cselect_b32 s21, s23, s21
	ds_read_b128 v[160:163], v10 offset:0
	ds_read_b128 v[164:167], v10 offset:2048
	ds_read_b128 v[168:171], v10 offset:4096
	ds_read_b128 v[172:175], v10 offset:6144
	ds_read_b128 v[176:179], v12 offset:0
	ds_read_b128 v[180:183], v12 offset:2048
	ds_read_b128 v[184:187], v12 offset:4096
	ds_read_b128 v[188:191], v12 offset:6144
	ds_read_b128 v[192:195], v12 offset:8192
	ds_read_b128 v[196:199], v12 offset:10240
	s_mov_b32 s15, 0
.Lou_loop:
	s_waitcnt lgkmcnt(0)
	v_mfma_f32_16x16x32_bf16 v[64:67], v[176:179], v[160:163], v[64:67]
	ds_read_b128 v[200:203], v11 offset:0
	v_mfma_f32_16x16x32_bf16 v[68:71], v[176:179], v[164:167], v[68:71]
	s_add_u32 m0, s20, 0x5000
	v_mfma_f32_16x16x32_bf16 v[72:75], v[176:179], v[168:171], v[72:75]
	ds_read_b128 v[204:207], v11 offset:2048
	v_mfma_f32_16x16x32_bf16 v[76:79], v[176:179], v[172:175], v[76:79]
	global_load_lds_dwordx4 v3, s[18:19]
	v_mfma_f32_16x16x32_bf16 v[80:83], v[180:183], v[160:163], v[80:83]
	ds_read_b128 v[208:211], v11 offset:4096
	v_mfma_f32_16x16x32_bf16 v[84:87], v[180:183], v[164:167], v[84:87]
	s_add_u32 m0, s20, 0x6000
	v_mfma_f32_16x16x32_bf16 v[88:91], v[180:183], v[168:171], v[88:91]
	ds_read_b128 v[212:215], v11 offset:6144
	v_mfma_f32_16x16x32_bf16 v[92:95], v[180:183], v[172:175], v[92:95]
	global_load_lds_dwordx4 v4, s[18:19]
	v_mfma_f32_16x16x32_bf16 v[96:99], v[184:187], v[160:163], v[96:99]
	ds_read_b128 v[216:219], v13 offset:0
	v_mfma_f32_16x16x32_bf16 v[100:103], v[184:187], v[164:167], v[100:103]
	s_add_u32 m0, s20, 0x7000
	v_mfma_f32_16x16x32_bf16 v[104:107], v[184:187], v[168:171], v[104:107]
	ds_read_b128 v[220:223], v13 offset:2048
	v_mfma_f32_16x16x32_bf16 v[108:111], v[184:187], v[172:175], v[108:111]
	global_load_lds_dwordx4 v5, s[18:19]
	v_mfma_f32_16x16x32_bf16 v[112:115], v[188:191], v[160:163], v[112:115]
	ds_read_b128 v[224:227], v13 offset:4096
	v_mfma_f32_16x16x32_bf16 v[116:119], v[188:191], v[164:167], v[116:119]
	s_add_u32 m0, s20, 0x8000
	v_mfma_f32_16x16x32_bf16 v[120:123], v[188:191], v[168:171], v[120:123]
	ds_read_b128 v[228:231], v13 offset:6144
	v_mfma_f32_16x16x32_bf16 v[124:127], v[188:191], v[172:175], v[124:127]
	global_load_lds_dwordx4 v6, s[18:19]
	v_mfma_f32_16x16x32_bf16 v[128:131], v[192:195], v[160:163], v[128:131]
	ds_read_b128 v[232:235], v13 offset:8192
	v_mfma_f32_16x16x32_bf16 v[132:135], v[192:195], v[164:167], v[132:135]
	s_add_u32 m0, s20, 0x9000
	v_mfma_f32_16x16x32_bf16 v[136:139], v[192:195], v[168:171], v[136:139]
	ds_read_b128 v[236:239], v13 offset:10240
	v_mfma_f32_16x16x32_bf16 v[140:143], v[192:195], v[172:175], v[140:143]
	global_load_lds_dwordx4 v7, s[18:19]
	v_mfma_f32_16x16x32_bf16 v[144:147], v[196:199], v[160:163], v[144:147]
	s_add_u32 s16, s16, 0x80
	s_addc_u32 s17, s17, 0
	s_add_u32 s18, s18, 0x80
	s_addc_u32 s19, s19, 0
	v_mfma_f32_16x16x32_bf16 v[148:151], v[196:199], v[164:167], v[148:151]
	s_add_u32 s20, s20, 0xa000
	s_sub_u32 s22, s20, 0x28000
	s_cmp_ge_u32 s20, 0x28000
	s_cselect_b32 s20, s22, s20
	v_mfma_f32_16x16x32_bf16 v[152:155], v[196:199], v[168:171], v[152:155]
	v_add_u32_e32 v10, s21, v8
	v_add_u32_e32 v12, s21, v9
	v_xor_b32_e32 v11, 64, v10
	v_xor_b32_e32 v13, 64, v12
	v_mfma_f32_16x16x32_bf16 v[156:159], v[196:199], v[172:175], v[156:159]
	s_add_u32 s21, s21, 0xa000
	s_sub_u32 s23, s21, 0x28000
	s_cmp_ge_u32 s21, 0x28000
	s_cselect_b32 s21, s23, s21
	s_waitcnt lgkmcnt(0)
	v_mfma_f32_16x16x32_bf16 v[64:67], v[216:219], v[200:203], v[64:67]
	v_mfma_f32_16x16x32_bf16 v[68:71], v[216:219], v[204:207], v[68:71]
	v_mfma_f32_16x16x32_bf16 v[72:75], v[216:219], v[208:211], v[72:75]
	v_mfma_f32_16x16x32_bf16 v[76:79], v[216:219], v[212:215], v[76:79]
	s_waitcnt vmcnt(20)
	s_barrier
	v_mfma_f32_16x16x32_bf16 v[80:83], v[220:223], v[200:203], v[80:83]
	ds_read_b128 v[160:163], v10 offset:0
	v_mfma_f32_16x16x32_bf16 v[84:87], v[220:223], v[204:207], v[84:87]
	s_add_u32 m0, s20, 0x0
	v_mfma_f32_16x16x32_bf16 v[88:91], v[220:223], v[208:211], v[88:91]
	ds_read_b128 v[164:167], v10 offset:2048
	v_mfma_f32_16x16x32_bf16 v[92:95], v[220:223], v[212:215], v[92:95]
	global_load_lds_dwordx4 v2, s[16:17]
	v_mfma_f32_16x16x32_bf16 v[96:99], v[224:227], v[200:203], v[96:99]
	ds_read_b128 v[168:171], v10 offset:4096
	v_mfma_f32_16x16x32_bf16 v[100:103], v[224:227], v[204:207], v[100:103]
	s_add_u32 m0, s20, 0x1000
	v_mfma_f32_16x16x32_bf16 v[104:107], v[224:227], v[208:211], v[104:107]
	ds_read_b128 v[172:175], v10 offset:6144
	v_mfma_f32_16x16x32_bf16 v[108:111], v[224:227], v[212:215], v[108:111]
	global_load_lds_dwordx4 v3, s[16:17]
	v_mfma_f32_16x16x32_bf16 v[112:115], v[228:231], v[200:203], v[112:115]
	ds_read_b128 v[176:179], v12 offset:0
	v_mfma_f32_16x16x32_bf16 v[116:119], v[228:231], v[204:207], v[116:119]
	s_add_u32 m0, s20, 0x2000
	v_mfma_f32_16x16x32_bf16 v[120:123], v[228:231], v[208:211], v[120:123]
	ds_read_b128 v[180:183], v12 offset:2048
	v_mfma_f32_16x16x32_bf16 v[124:127], v[228:231], v[212:215], v[124:127]
	global_load_lds_dwordx4 v4, s[16:17]
	v_mfma_f32_16x16x32_bf16 v[128:131], v[232:235], v[200:203], v[128:131]
	ds_read_b128 v[184:187], v12 offset:4096
	v_mfma_f32_16x16x32_bf16 v[132:135], v[232:235], v[204:207], v[132:135]
	s_add_u32 m0, s20, 0x3000
	v_mfma_f32_16x16x32_bf16 v[136:139], v[232:235], v[208:211], v[136:139]
	ds_read_b128 v[188:191], v12 offset:6144
	v_mfma_f32_16x16x32_bf16 v[140:143], v[232:235], v[212:215], v[140:143]
	global_load_lds_dwordx4 v5, s[16:17]
	v_mfma_f32_16x16x32_bf16 v[144:147], v[236:239], v[200:203], v[144:147]
	ds_read_b128 v[192:195], v12 offset:8192
	v_mfma_f32_16x16x32_bf16 v[148:151], v[236:239], v[204:207], v[148:151]
	s_add_u32 m0, s20, 0x4000
	v_mfma_f32_16x16x32_bf16 v[152:155], v[236:239], v[208:211], v[152:155]
	ds_read_b128 v[196:199], v12 offset:10240
	v_mfma_f32_16x16x32_bf16 v[156:159], v[236:239], v[212:215], v[156:159]
	global_load_lds_dwordx4 v2, s[18:19]
	s_add_u32 s15, s15, 1
	s_cmp_lt_u32 s15, 8
	s_cbranch_scc1 .Lou_loop
	s_waitcnt lgkmcnt(0)
	v_mfma_f32_16x16x32_bf16 v[64:67], v[176:179], v[160:163], v[64:67]
	ds_read_b128 v[200:203], v11 offset:0
	v_mfma_f32_16x16x32_bf16 v[68:71], v[176:179], v[164:167], v[68:71]
	s_add_u32 m0, s20, 0x5000
	v_mfma_f32_16x16x32_bf16 v[72:75], v[176:179], v[168:171], v[72:75]
	ds_read_b128 v[204:207], v11 offset:2048
	v_mfma_f32_16x16x32_bf16 v[76:79], v[176:179], v[172:175], v[76:79]
	global_load_lds_dwordx4 v3, s[18:19]
	v_mfma_f32_16x16x32_bf16 v[80:83], v[180:183], v[160:163], v[80:83]
	ds_read_b128 v[208:211], v11 offset:4096
	v_mfma_f32_16x16x32_bf16 v[84:87], v[180:183], v[164:167], v[84:87]
	s_add_u32 m0, s20, 0x6000
	v_mfma_f32_16x16x32_bf16 v[88:91], v[180:183], v[168:171], v[88:91]
	ds_read_b128 v[212:215], v11 offset:6144
	v_mfma_f32_16x16x32_bf16 v[92:95], v[180:183], v[172:175], v[92:95]
	global_load_lds_dwordx4 v4, s[18:19]
	v_mfma_f32_16x16x32_bf16 v[96:99], v[184:187], v[160:163], v[96:99]
	ds_read_b128 v[216:219], v13 offset:0
	v_mfma_f32_16x16x32_bf16 v[100:103], v[184:187], v[164:167], v[100:103]
	s_add_u32 m0, s20, 0x7000
	v_mfma_f32_16x16x32_bf16 v[104:107], v[184:187], v[168:171], v[104:107]
	ds_read_b128 v[220:223], v13 offset:2048
	v_mfma_f32_16x16x32_bf16 v[108:111], v[184:187], v[172:175], v[108:111]
	global_load_lds_dwordx4 v5, s[18:19]
	v_mfma_f32_16x16x32_bf16 v[112:115], v[188:191], v[160:163], v[112:115]
	ds_read_b128 v[224:227], v13 offset:4096
	v_mfma_f32_16x16x32_bf16 v[116:119], v[188:191], v[164:167], v[116:119]
	s_add_u32 m0, s20, 0x8000
	v_mfma_f32_16x16x32_bf16 v[120:123], v[188:191], v[168:171], v[120:123]
	ds_read_b128 v[228:231], v13 offset:6144
	v_mfma_f32_16x16x32_bf16 v[124:127], v[188:191], v[172:175], v[124:127]
	global_load_lds_dwordx4 v6, s[18:19]
	v_mfma_f32_16x16x32_bf16 v[128:131], v[192:195], v[160:163], v[128:131]
	ds_read_b128 v[232:235], v13 offset:8192
	v_mfma_f32_16x16x32_bf16 v[132:135], v[192:195], v[164:167], v[132:135]
	s_add_u32 m0, s20, 0x9000
	v_mfma_f32_16x16x32_bf16 v[136:139], v[192:195], v[168:171], v[136:139]
	ds_read_b128 v[236:239], v13 offset:10240
	v_mfma_f32_16x16x32_bf16 v[140:143], v[192:195], v[172:175], v[140:143]
	global_load_lds_dwordx4 v7, s[18:19]
	v_mfma_f32_16x16x32_bf16 v[144:147], v[196:199], v[160:163], v[144:147]
	s_add_u32 s16, s16, 0x80
	s_addc_u32 s17, s17, 0
	s_add_u32 s18, s18, 0x80
	s_addc_u32 s19, s19, 0
	v_mfma_f32_16x16x32_bf16 v[148:151], v[196:199], v[164:167], v[148:151]
	s_add_u32 s20, s20, 0xa000
	s_sub_u32 s22, s20, 0x28000
	s_cmp_ge_u32 s20, 0x28000
	s_cselect_b32 s20, s22, s20
	v_mfma_f32_16x16x32_bf16 v[152:155], v[196:199], v[168:171], v[152:155]
	v_add_u32_e32 v10, s21, v8
	v_add_u32_e32 v12, s21, v9
	v_xor_b32_e32 v11, 64, v10
	v_xor_b32_e32 v13, 64, v12
	v_mfma_f32_16x16x32_bf16 v[156:159], v[196:199], v[172:175], v[156:159]
	s_add_u32 s21, s21, 0xa000
	s_sub_u32 s23, s21, 0x28000
	s_cmp_ge_u32 s21, 0x28000
	s_cselect_b32 s21, s23, s21
	s_waitcnt lgkmcnt(0)
	v_mfma_f32_16x16x32_bf16 v[64:67], v[216:219], v[200:203], v[64:67]
	v_mfma_f32_16x16x32_bf16 v[68:71], v[216:219], v[204:207], v[68:71]
	v_mfma_f32_16x16x32_bf16 v[72:75], v[216:219], v[208:211], v[72:75]
	v_mfma_f32_16x16x32_bf16 v[76:79], v[216:219], v[212:215], v[76:79]
	s_waitcnt vmcnt(20)
	s_barrier
	v_mfma_f32_16x16x32_bf16 v[80:83], v[220:223], v[200:203], v[80:83]
	ds_read_b128 v[160:163], v10 offset:0
	v_mfma_f32_16x16x32_bf16 v[84:87], v[220:223], v[204:207], v[84:87]
	global_load_dwordx4 v[240:243], v60, s[24:25]
	v_mfma_f32_16x16x32_bf16 v[88:91], v[220:223], v[208:211], v[88:91]
	ds_read_b128 v[164:167], v10 offset:2048
	v_mfma_f32_16x16x32_bf16 v[92:95], v[220:223], v[212:215], v[92:95]
	global_load_dwordx4 v[244:247], v60, s[24:25] offset:64
	v_mfma_f32_16x16x32_bf16 v[96:99], v[224:227], v[200:203], v[96:99]
	ds_read_b128 v[168:171], v10 offset:4096
	v_mfma_f32_16x16x32_bf16 v[100:103], v[224:227], v[204:207], v[100:103]
	global_load_dwordx4 v[248:251], v60, s[24:25] offset:128
	v_mfma_f32_16x16x32_bf16 v[104:107], v[224:227], v[208:211], v[104:107]
	ds_read_b128 v[172:175], v10 offset:6144
	v_mfma_f32_16x16x32_bf16 v[108:111], v[224:227], v[212:215], v[108:111]
	global_load_dwordx4 v[252:255], v60, s[24:25] offset:192
	v_mfma_f32_16x16x32_bf16 v[112:115], v[228:231], v[200:203], v[112:115]
	ds_read_b128 v[176:179], v12 offset:0
	v_mfma_f32_16x16x32_bf16 v[116:119], v[228:231], v[204:207], v[116:119]
	global_load_dwordx4 v[48:51], v60, s[24:25] offset:256
	v_mfma_f32_16x16x32_bf16 v[120:123], v[228:231], v[208:211], v[120:123]
	ds_read_b128 v[180:183], v12 offset:2048
	v_mfma_f32_16x16x32_bf16 v[124:127], v[228:231], v[212:215], v[124:127]
	global_load_dwordx4 v[52:55], v60, s[24:25] offset:320
	v_mfma_f32_16x16x32_bf16 v[128:131], v[232:235], v[200:203], v[128:131]
	ds_read_b128 v[184:187], v12 offset:4096
	v_mfma_f32_16x16x32_bf16 v[132:135], v[232:235], v[204:207], v[132:135]
	global_load_dwordx4 v[16:19], v56, s[8:9] offset:0
	v_mfma_f32_16x16x32_bf16 v[136:139], v[232:235], v[208:211], v[136:139]
	ds_read_b128 v[188:191], v12 offset:6144
	v_mfma_f32_16x16x32_bf16 v[140:143], v[232:235], v[212:215], v[140:143]
	global_load_dwordx4 v[20:23], v56, s[8:9] offset:64
	v_mfma_f32_16x16x32_bf16 v[144:147], v[236:239], v[200:203], v[144:147]
	ds_read_b128 v[192:195], v12 offset:8192
	v_mfma_f32_16x16x32_bf16 v[148:151], v[236:239], v[204:207], v[148:151]
	global_load_dwordx4 v[24:27], v56, s[8:9] offset:128
	v_mfma_f32_16x16x32_bf16 v[152:155], v[236:239], v[208:211], v[152:155]
	ds_read_b128 v[196:199], v12 offset:10240
	v_mfma_f32_16x16x32_bf16 v[156:159], v[236:239], v[212:215], v[156:159]
	global_load_dwordx4 v[28:31], v56, s[8:9] offset:192
	global_load_dwordx4 v[32:35], v56, s[8:9] offset:256
	global_load_dwordx4 v[36:39], v56, s[8:9] offset:320
	global_load_dwordx4 v[40:43], v57, s[8:9] offset:0
	global_load_dwordx4 v[44:47], v57, s[8:9] offset:64
	s_waitcnt lgkmcnt(0)
	v_mfma_f32_16x16x32_bf16 v[64:67], v[176:179], v[160:163], v[64:67]
	ds_read_b128 v[200:203], v11 offset:0
	v_mfma_f32_16x16x32_bf16 v[68:71], v[176:179], v[164:167], v[68:71]
	ds_read_b128 v[204:207], v11 offset:2048
	v_mfma_f32_16x16x32_bf16 v[72:75], v[176:179], v[168:171], v[72:75]
	ds_read_b128 v[208:211], v11 offset:4096
	v_mfma_f32_16x16x32_bf16 v[76:79], v[176:179], v[172:175], v[76:79]
	ds_read_b128 v[212:215], v11 offset:6144
	v_mfma_f32_16x16x32_bf16 v[80:83], v[180:183], v[160:163], v[80:83]
	ds_read_b128 v[216:219], v13 offset:0
	v_mfma_f32_16x16x32_bf16 v[84:87], v[180:183], v[164:167], v[84:87]
	ds_read_b128 v[220:223], v13 offset:2048
	v_mfma_f32_16x16x32_bf16 v[88:91], v[180:183], v[168:171], v[88:91]
	ds_read_b128 v[224:227], v13 offset:4096
	v_mfma_f32_16x16x32_bf16 v[92:95], v[180:183], v[172:175], v[92:95]
	ds_read_b128 v[228:231], v13 offset:6144
	v_mfma_f32_16x16x32_bf16 v[96:99], v[184:187], v[160:163], v[96:99]
	ds_read_b128 v[232:235], v13 offset:8192
	v_mfma_f32_16x16x32_bf16 v[100:103], v[184:187], v[164:167], v[100:103]
	ds_read_b128 v[236:239], v13 offset:10240
	v_mfma_f32_16x16x32_bf16 v[104:107], v[184:187], v[168:171], v[104:107]
	v_mfma_f32_16x16x32_bf16 v[108:111], v[184:187], v[172:175], v[108:111]
	v_mfma_f32_16x16x32_bf16 v[112:115], v[188:191], v[160:163], v[112:115]
	v_mfma_f32_16x16x32_bf16 v[116:119], v[188:191], v[164:167], v[116:119]
	v_mfma_f32_16x16x32_bf16 v[120:123], v[188:191], v[168:171], v[120:123]
	v_mfma_f32_16x16x32_bf16 v[124:127], v[188:191], v[172:175], v[124:127]
	v_mfma_f32_16x16x32_bf16 v[128:131], v[192:195], v[160:163], v[128:131]
	v_mfma_f32_16x16x32_bf16 v[132:135], v[192:195], v[164:167], v[132:135]
	v_mfma_f32_16x16x32_bf16 v[136:139], v[192:195], v[168:171], v[136:139]
	v_mfma_f32_16x16x32_bf16 v[140:143], v[192:195], v[172:175], v[140:143]
	v_mfma_f32_16x16x32_bf16 v[144:147], v[196:199], v[160:163], v[144:147]
	v_add_u32_e32 v10, s21, v8
	v_add_u32_e32 v12, s21, v9
	v_xor_b32_e32 v11, 64, v10
	v_xor_b32_e32 v13, 64, v12
	v_mfma_f32_16x16x32_bf16 v[148:151], v[196:199], v[164:167], v[148:151]
	s_add_u32 s21, s21, 0xa000
	s_sub_u32 s23, s21, 0x28000
	s_cmp_ge_u32 s21, 0x28000
	s_cselect_b32 s21, s23, s21
	v_mfma_f32_16x16x32_bf16 v[152:155], v[196:199], v[168:171], v[152:155]
	v_mfma_f32_16x16x32_bf16 v[156:159], v[196:199], v[172:175], v[156:159]
	s_waitcnt lgkmcnt(0)
	v_mfma_f32_16x16x32_bf16 v[64:67], v[216:219], v[200:203], v[64:67]
	v_mfma_f32_16x16x32_bf16 v[68:71], v[216:219], v[204:207], v[68:71]
	v_mfma_f32_16x16x32_bf16 v[72:75], v[216:219], v[208:211], v[72:75]
	v_mfma_f32_16x16x32_bf16 v[76:79], v[216:219], v[212:215], v[76:79]
	s_waitcnt vmcnt(24)
	s_barrier
	v_mfma_f32_16x16x32_bf16 v[80:83], v[220:223], v[200:203], v[80:83]
	ds_read_b128 v[160:163], v10 offset:0
	v_mfma_f32_16x16x32_bf16 v[84:87], v[220:223], v[204:207], v[84:87]
	ds_read_b128 v[164:167], v10 offset:2048
	v_mfma_f32_16x16x32_bf16 v[88:91], v[220:223], v[208:211], v[88:91]
	ds_read_b128 v[168:171], v10 offset:4096
	v_mfma_f32_16x16x32_bf16 v[92:95], v[220:223], v[212:215], v[92:95]
	ds_read_b128 v[172:175], v10 offset:6144
	v_mfma_f32_16x16x32_bf16 v[96:99], v[224:227], v[200:203], v[96:99]
	ds_read_b128 v[176:179], v12 offset:0
	v_mfma_f32_16x16x32_bf16 v[100:103], v[224:227], v[204:207], v[100:103]
	ds_read_b128 v[180:183], v12 offset:2048
	v_mfma_f32_16x16x32_bf16 v[104:107], v[224:227], v[208:211], v[104:107]
	ds_read_b128 v[184:187], v12 offset:4096
	v_mfma_f32_16x16x32_bf16 v[108:111], v[224:227], v[212:215], v[108:111]
	ds_read_b128 v[188:191], v12 offset:6144
	v_mfma_f32_16x16x32_bf16 v[112:115], v[228:231], v[200:203], v[112:115]
	ds_read_b128 v[192:195], v12 offset:8192
	v_mfma_f32_16x16x32_bf16 v[116:119], v[228:231], v[204:207], v[116:119]
	ds_read_b128 v[196:199], v12 offset:10240
	v_mfma_f32_16x16x32_bf16 v[120:123], v[228:231], v[208:211], v[120:123]
	v_mfma_f32_16x16x32_bf16 v[124:127], v[228:231], v[212:215], v[124:127]
	v_mfma_f32_16x16x32_bf16 v[128:131], v[232:235], v[200:203], v[128:131]
	v_mfma_f32_16x16x32_bf16 v[132:135], v[232:235], v[204:207], v[132:135]
	v_mfma_f32_16x16x32_bf16 v[136:139], v[232:235], v[208:211], v[136:139]
	v_mfma_f32_16x16x32_bf16 v[140:143], v[232:235], v[212:215], v[140:143]
	v_mfma_f32_16x16x32_bf16 v[144:147], v[236:239], v[200:203], v[144:147]
	v_mfma_f32_16x16x32_bf16 v[148:151], v[236:239], v[204:207], v[148:151]
	v_mfma_f32_16x16x32_bf16 v[152:155], v[236:239], v[208:211], v[152:155]
	v_mfma_f32_16x16x32_bf16 v[156:159], v[236:239], v[212:215], v[156:159]
	s_waitcnt lgkmcnt(0)
	v_mfma_f32_16x16x32_bf16 v[64:67], v[176:179], v[160:163], v[64:67]
	ds_read_b128 v[200:203], v11 offset:0
	v_mfma_f32_16x16x32_bf16 v[68:71], v[176:179], v[164:167], v[68:71]
	ds_read_b128 v[204:207], v11 offset:2048
	v_mfma_f32_16x16x32_bf16 v[72:75], v[176:179], v[168:171], v[72:75]
	ds_read_b128 v[208:211], v11 offset:4096
	v_mfma_f32_16x16x32_bf16 v[76:79], v[176:179], v[172:175], v[76:79]
	ds_read_b128 v[212:215], v11 offset:6144
	v_mfma_f32_16x16x32_bf16 v[80:83], v[180:183], v[160:163], v[80:83]
	ds_read_b128 v[216:219], v13 offset:0
	v_mfma_f32_16x16x32_bf16 v[84:87], v[180:183], v[164:167], v[84:87]
	ds_read_b128 v[220:223], v13 offset:2048
	v_mfma_f32_16x16x32_bf16 v[88:91], v[180:183], v[168:171], v[88:91]
	ds_read_b128 v[224:227], v13 offset:4096
	v_mfma_f32_16x16x32_bf16 v[92:95], v[180:183], v[172:175], v[92:95]
	ds_read_b128 v[228:231], v13 offset:6144
	v_mfma_f32_16x16x32_bf16 v[96:99], v[184:187], v[160:163], v[96:99]
	ds_read_b128 v[232:235], v13 offset:8192
	v_mfma_f32_16x16x32_bf16 v[100:103], v[184:187], v[164:167], v[100:103]
	ds_read_b128 v[236:239], v13 offset:10240
	v_mfma_f32_16x16x32_bf16 v[104:107], v[184:187], v[168:171], v[104:107]
	v_mfma_f32_16x16x32_bf16 v[108:111], v[184:187], v[172:175], v[108:111]
	v_mfma_f32_16x16x32_bf16 v[112:115], v[188:191], v[160:163], v[112:115]
	v_mfma_f32_16x16x32_bf16 v[116:119], v[188:191], v[164:167], v[116:119]
	v_mfma_f32_16x16x32_bf16 v[120:123], v[188:191], v[168:171], v[120:123]
	v_mfma_f32_16x16x32_bf16 v[124:127], v[188:191], v[172:175], v[124:127]
	v_mfma_f32_16x16x32_bf16 v[128:131], v[192:195], v[160:163], v[128:131]
	v_mfma_f32_16x16x32_bf16 v[132:135], v[192:195], v[164:167], v[132:135]
	v_mfma_f32_16x16x32_bf16 v[136:139], v[192:195], v[168:171], v[136:139]
	v_mfma_f32_16x16x32_bf16 v[140:143], v[192:195], v[172:175], v[140:143]
	v_mfma_f32_16x16x32_bf16 v[144:147], v[196:199], v[160:163], v[144:147]
	v_add_u32_e32 v10, s21, v8
	v_add_u32_e32 v12, s21, v9
	v_xor_b32_e32 v11, 64, v10
	v_xor_b32_e32 v13, 64, v12
	v_mfma_f32_16x16x32_bf16 v[148:151], v[196:199], v[164:167], v[148:151]
	s_add_u32 s21, s21, 0xa000
	s_sub_u32 s23, s21, 0x28000
	s_cmp_ge_u32 s21, 0x28000
	s_cselect_b32 s21, s23, s21
	v_mfma_f32_16x16x32_bf16 v[152:155], v[196:199], v[168:171], v[152:155]
	v_mfma_f32_16x16x32_bf16 v[156:159], v[196:199], v[172:175], v[156:159]
	s_waitcnt lgkmcnt(0)
	v_mfma_f32_16x16x32_bf16 v[64:67], v[216:219], v[200:203], v[64:67]
	v_mfma_f32_16x16x32_bf16 v[68:71], v[216:219], v[204:207], v[68:71]
	v_mfma_f32_16x16x32_bf16 v[72:75], v[216:219], v[208:211], v[72:75]
	v_mfma_f32_16x16x32_bf16 v[76:79], v[216:219], v[212:215], v[76:79]
	s_waitcnt vmcnt(14)
	s_barrier
	v_mfma_f32_16x16x32_bf16 v[80:83], v[220:223], v[200:203], v[80:83]
	ds_read_b128 v[160:163], v10 offset:0
	v_mfma_f32_16x16x32_bf16 v[84:87], v[220:223], v[204:207], v[84:87]
	ds_read_b128 v[164:167], v10 offset:2048
	v_mfma_f32_16x16x32_bf16 v[88:91], v[220:223], v[208:211], v[88:91]
	ds_read_b128 v[168:171], v10 offset:4096
	v_mfma_f32_16x16x32_bf16 v[92:95], v[220:223], v[212:215], v[92:95]
	ds_read_b128 v[172:175], v10 offset:6144
	v_mfma_f32_16x16x32_bf16 v[96:99], v[224:227], v[200:203], v[96:99]
	ds_read_b128 v[176:179], v12 offset:0
	v_mfma_f32_16x16x32_bf16 v[100:103], v[224:227], v[204:207], v[100:103]
	ds_read_b128 v[180:183], v12 offset:2048
	v_mfma_f32_16x16x32_bf16 v[104:107], v[224:227], v[208:211], v[104:107]
	ds_read_b128 v[184:187], v12 offset:4096
	v_mfma_f32_16x16x32_bf16 v[108:111], v[224:227], v[212:215], v[108:111]
	ds_read_b128 v[188:191], v12 offset:6144
	v_mfma_f32_16x16x32_bf16 v[112:115], v[228:231], v[200:203], v[112:115]
	ds_read_b128 v[192:195], v12 offset:8192
	v_mfma_f32_16x16x32_bf16 v[116:119], v[228:231], v[204:207], v[116:119]
	ds_read_b128 v[196:199], v12 offset:10240
	v_mfma_f32_16x16x32_bf16 v[120:123], v[228:231], v[208:211], v[120:123]
	v_mfma_f32_16x16x32_bf16 v[124:127], v[228:231], v[212:215], v[124:127]
	v_mfma_f32_16x16x32_bf16 v[128:131], v[232:235], v[200:203], v[128:131]
	v_mfma_f32_16x16x32_bf16 v[132:135], v[232:235], v[204:207], v[132:135]
	v_mfma_f32_16x16x32_bf16 v[136:139], v[232:235], v[208:211], v[136:139]
	v_mfma_f32_16x16x32_bf16 v[140:143], v[232:235], v[212:215], v[140:143]
	v_mfma_f32_16x16x32_bf16 v[144:147], v[236:239], v[200:203], v[144:147]
	v_mfma_f32_16x16x32_bf16 v[148:151], v[236:239], v[204:207], v[148:151]
	v_mfma_f32_16x16x32_bf16 v[152:155], v[236:239], v[208:211], v[152:155]
	v_mfma_f32_16x16x32_bf16 v[156:159], v[236:239], v[212:215], v[156:159]
	s_waitcnt lgkmcnt(0)
	v_mfma_f32_16x16x32_bf16 v[64:67], v[176:179], v[160:163], v[64:67]
	ds_read_b128 v[200:203], v11 offset:0
	v_mfma_f32_16x16x32_bf16 v[68:71], v[176:179], v[164:167], v[68:71]
	ds_read_b128 v[204:207], v11 offset:2048
	v_mfma_f32_16x16x32_bf16 v[72:75], v[176:179], v[168:171], v[72:75]
	ds_read_b128 v[208:211], v11 offset:4096
	v_mfma_f32_16x16x32_bf16 v[76:79], v[176:179], v[172:175], v[76:79]
	ds_read_b128 v[212:215], v11 offset:6144
	v_mfma_f32_16x16x32_bf16 v[80:83], v[180:183], v[160:163], v[80:83]
	ds_read_b128 v[216:219], v13 offset:0
	v_mfma_f32_16x16x32_bf16 v[84:87], v[180:183], v[164:167], v[84:87]
	ds_read_b128 v[220:223], v13 offset:2048
	v_mfma_f32_16x16x32_bf16 v[88:91], v[180:183], v[168:171], v[88:91]
	ds_read_b128 v[224:227], v13 offset:4096
	v_mfma_f32_16x16x32_bf16 v[92:95], v[180:183], v[172:175], v[92:95]
	ds_read_b128 v[228:231], v13 offset:6144
	v_mfma_f32_16x16x32_bf16 v[96:99], v[184:187], v[160:163], v[96:99]
	ds_read_b128 v[232:235], v13 offset:8192
	v_mfma_f32_16x16x32_bf16 v[100:103], v[184:187], v[164:167], v[100:103]
	ds_read_b128 v[236:239], v13 offset:10240
	v_mfma_f32_16x16x32_bf16 v[104:107], v[184:187], v[168:171], v[104:107]
	v_mfma_f32_16x16x32_bf16 v[108:111], v[184:187], v[172:175], v[108:111]
	v_mfma_f32_16x16x32_bf16 v[112:115], v[188:191], v[160:163], v[112:115]
	v_mfma_f32_16x16x32_bf16 v[116:119], v[188:191], v[164:167], v[116:119]
	v_mfma_f32_16x16x32_bf16 v[120:123], v[188:191], v[168:171], v[120:123]
	v_mfma_f32_16x16x32_bf16 v[124:127], v[188:191], v[172:175], v[124:127]
	v_mfma_f32_16x16x32_bf16 v[128:131], v[192:195], v[160:163], v[128:131]
	v_mfma_f32_16x16x32_bf16 v[132:135], v[192:195], v[164:167], v[132:135]
	v_mfma_f32_16x16x32_bf16 v[136:139], v[192:195], v[168:171], v[136:139]
	v_mfma_f32_16x16x32_bf16 v[140:143], v[192:195], v[172:175], v[140:143]
	v_mfma_f32_16x16x32_bf16 v[144:147], v[196:199], v[160:163], v[144:147]
	v_mfma_f32_16x16x32_bf16 v[148:151], v[196:199], v[164:167], v[148:151]
	v_mfma_f32_16x16x32_bf16 v[152:155], v[196:199], v[168:171], v[152:155]
	v_mfma_f32_16x16x32_bf16 v[156:159], v[196:199], v[172:175], v[156:159]
	s_waitcnt lgkmcnt(0)
	v_mfma_f32_16x16x32_bf16 v[64:67], v[216:219], v[200:203], v[64:67]
	v_mfma_f32_16x16x32_bf16 v[68:71], v[216:219], v[204:207], v[68:71]
	global_load_dwordx4 v[160:163], v57, s[8:9] offset:128
	v_mfma_f32_16x16x32_bf16 v[72:75], v[216:219], v[208:211], v[72:75]
	v_mfma_f32_16x16x32_bf16 v[76:79], v[216:219], v[212:215], v[76:79]
	global_load_dwordx4 v[164:167], v57, s[8:9] offset:192
	v_mfma_f32_16x16x32_bf16 v[80:83], v[220:223], v[200:203], v[80:83]
	v_mfma_f32_16x16x32_bf16 v[84:87], v[220:223], v[204:207], v[84:87]
	global_load_dwordx4 v[168:171], v57, s[8:9] offset:256
	v_mfma_f32_16x16x32_bf16 v[88:91], v[220:223], v[208:211], v[88:91]
	v_mfma_f32_16x16x32_bf16 v[92:95], v[220:223], v[212:215], v[92:95]
	global_load_dwordx4 v[172:175], v57, s[8:9] offset:320
	v_mfma_f32_16x16x32_bf16 v[96:99], v[224:227], v[200:203], v[96:99]
	v_mfma_f32_16x16x32_bf16 v[100:103], v[224:227], v[204:207], v[100:103]
	global_load_dwordx4 v[176:179], v58, s[8:9] offset:0
	v_mfma_f32_16x16x32_bf16 v[104:107], v[224:227], v[208:211], v[104:107]
	v_mfma_f32_16x16x32_bf16 v[108:111], v[224:227], v[212:215], v[108:111]
	global_load_dwordx4 v[180:183], v58, s[8:9] offset:64
	v_mfma_f32_16x16x32_bf16 v[112:115], v[228:231], v[200:203], v[112:115]
	v_mfma_f32_16x16x32_bf16 v[116:119], v[228:231], v[204:207], v[116:119]
	global_load_dwordx4 v[184:187], v58, s[8:9] offset:128
	v_mfma_f32_16x16x32_bf16 v[120:123], v[228:231], v[208:211], v[120:123]
	v_mfma_f32_16x16x32_bf16 v[124:127], v[228:231], v[212:215], v[124:127]
	global_load_dwordx4 v[188:191], v58, s[8:9] offset:192
	v_mfma_f32_16x16x32_bf16 v[128:131], v[232:235], v[200:203], v[128:131]
	v_mfma_f32_16x16x32_bf16 v[132:135], v[232:235], v[204:207], v[132:135]
	global_load_dwordx4 v[192:195], v58, s[8:9] offset:256
	v_mfma_f32_16x16x32_bf16 v[136:139], v[232:235], v[208:211], v[136:139]
	v_mfma_f32_16x16x32_bf16 v[140:143], v[232:235], v[212:215], v[140:143]
	global_load_dwordx4 v[196:199], v58, s[8:9] offset:320
	v_mfma_f32_16x16x32_bf16 v[144:147], v[236:239], v[200:203], v[144:147]
	v_mfma_f32_16x16x32_bf16 v[148:151], v[236:239], v[204:207], v[148:151]
	v_mfma_f32_16x16x32_bf16 v[152:155], v[236:239], v[208:211], v[152:155]
	v_mfma_f32_16x16x32_bf16 v[156:159], v[236:239], v[212:215], v[156:159]
	v_and_b32_e32 v12, 63, v0
	v_cmp_gt_u32_e32 vcc, 16, v12
	v_xor_b32_e32 v13, 16, v12
	v_lshlrev_b32_e32 v13, 2, v13
	v_xor_b32_e32 v12, 32, v12
	v_lshlrev_b32_e32 v12, 2, v12
	v_bfe_u32 v14, v0, 6, 1
	v_mul_u32_u24_e32 v14, 0x60, v14
	v_bfe_u32 v15, v0, 4, 2
	v_lshl_add_u32 v14, v15, 2, v14
	v_add_u32_e32 v14, s13, v14
	v_lshlrev_b32_e32 v14, 2, v14
	global_load_dwordx4 v[200:203], v59, s[8:9] offset:0
	global_load_dwordx4 v[204:207], v59, s[8:9] offset:64
	global_load_dwordx4 v[208:211], v59, s[8:9] offset:128
	global_load_dwordx4 v[212:215], v59, s[8:9] offset:192
	global_load_dwordx4 v[216:219], v59, s[8:9] offset:256
	global_load_dwordx4 v[220:223], v59, s[8:9] offset:320
	v_lshrrev_b32_e32 v60, 1, v56
	v_lshrrev_b32_e32 v61, 1, v57
	v_lshrrev_b32_e32 v62, 1, v58
	v_lshrrev_b32_e32 v63, 1, v59
	v_bfe_u32 v8, v0, 7, 1
	v_and_b32_e32 v9, 15, v0
	v_lshl_add_u32 v8, v8, 6, v9
	v_add_u32_e32 v8, s12, v8
	v_lshlrev_b32_e32 v8, 6, v8
	v_bfe_u32 v9, v0, 6, 1
	v_lshlrev_b32_e32 v9, 1, v9
	v_add_u32_e32 v9, s30, v9
	v_lshl_add_u32 v8, v9, 2, v8
	v_add_u32_e32 v9, 0x400, v8
	v_add_u32_e32 v10, 0x400, v9
	v_add_u32_e32 v11, 0x400, v10
	s_waitcnt vmcnt(23)
	v_pk_add_f32 v[64:65], v[64:65], v[16:17]
	v_pk_add_f32 v[66:67], v[66:67], v[18:19]
	global_store_dwordx4 v56, v[64:67], s[10:11]
	v_pk_mul_f32 v[224:225], v[240:241], v[64:65]
	v_pk_mul_f32 v[226:227], v[242:243], v[66:67]
	v_cvt_pk_bf16_f32 v228, v224, v225
	v_cvt_pk_bf16_f32 v229, v226, v227
	global_store_dwordx2 v60, v[228:229], s[28:29]
	v_pk_mul_f32 v[230:231], v[64:65], v[64:65]
	v_pk_mul_f32 v[232:233], v[66:67], v[66:67]
	v_add_f32_e32 v230, v230, v231
	v_add_f32_e32 v230, v232, v230
	v_add_f32_e32 v234, v233, v230
	s_waitcnt vmcnt(24)
	v_pk_add_f32 v[80:81], v[80:81], v[20:21]
	v_pk_add_f32 v[82:83], v[82:83], v[22:23]
	global_store_dwordx4 v56, v[80:83], s[10:11] offset:64
	v_pk_mul_f32 v[224:225], v[244:245], v[80:81]
	v_pk_mul_f32 v[226:227], v[246:247], v[82:83]
	v_cvt_pk_bf16_f32 v228, v224, v225
	v_cvt_pk_bf16_f32 v229, v226, v227
	global_store_dwordx2 v60, v[228:229], s[28:29] offset:32
	v_pk_mul_f32 v[230:231], v[80:81], v[80:81]
	v_pk_mul_f32 v[232:233], v[82:83], v[82:83]
	v_add_f32_e32 v230, v230, v231
	v_add_f32_e32 v230, v232, v230
	v_add_f32_e32 v230, v233, v230
	v_add_f32_e32 v234, v234, v230
	s_waitcnt vmcnt(25)
	v_pk_add_f32 v[96:97], v[96:97], v[24:25]
	v_pk_add_f32 v[98:99], v[98:99], v[26:27]
	global_store_dwordx4 v56, v[96:99], s[10:11] offset:128
	v_pk_mul_f32 v[224:225], v[248:249], v[96:97]
	v_pk_mul_f32 v[226:227], v[250:251], v[98:99]
	v_cvt_pk_bf16_f32 v228, v224, v225
	v_cvt_pk_bf16_f32 v229, v226, v227
	global_store_dwordx2 v60, v[228:229], s[28:29] offset:64
	v_pk_mul_f32 v[230:231], v[96:97], v[96:97]
	v_pk_mul_f32 v[232:233], v[98:99], v[98:99]
	v_add_f32_e32 v230, v230, v231
	v_add_f32_e32 v230, v232, v230
	v_add_f32_e32 v230, v233, v230
	v_add_f32_e32 v234, v234, v230
	s_waitcnt vmcnt(26)
	v_pk_add_f32 v[112:113], v[112:113], v[28:29]
	v_pk_add_f32 v[114:115], v[114:115], v[30:31]
	global_store_dwordx4 v56, v[112:115], s[10:11] offset:192
	v_pk_mul_f32 v[224:225], v[252:253], v[112:113]
	v_pk_mul_f32 v[226:227], v[254:255], v[114:115]
	v_cvt_pk_bf16_f32 v228, v224, v225
	v_cvt_pk_bf16_f32 v229, v226, v227
	global_store_dwordx2 v60, v[228:229], s[28:29] offset:96
	v_pk_mul_f32 v[230:231], v[112:113], v[112:113]
	v_pk_mul_f32 v[232:233], v[114:115], v[114:115]
	v_add_f32_e32 v230, v230, v231
	v_add_f32_e32 v230, v232, v230
	v_add_f32_e32 v235, v233, v230
	s_waitcnt vmcnt(27)
	v_pk_add_f32 v[128:129], v[128:129], v[32:33]
	v_pk_add_f32 v[130:131], v[130:131], v[34:35]
	global_store_dwordx4 v56, v[128:131], s[10:11] offset:256
	v_pk_mul_f32 v[224:225], v[48:49], v[128:129]
	v_pk_mul_f32 v[226:227], v[50:51], v[130:131]
	v_cvt_pk_bf16_f32 v228, v224, v225
	v_cvt_pk_bf16_f32 v229, v226, v227
	global_store_dwordx2 v60, v[228:229], s[28:29] offset:128
	v_pk_mul_f32 v[230:231], v[128:129], v[128:129]
	v_pk_mul_f32 v[232:233], v[130:131], v[130:131]
	v_add_f32_e32 v230, v230, v231
	v_add_f32_e32 v230, v232, v230
	v_add_f32_e32 v230, v233, v230
	v_add_f32_e32 v235, v235, v230
	s_waitcnt vmcnt(28)
	v_pk_add_f32 v[144:145], v[144:145], v[36:37]
	v_pk_add_f32 v[146:147], v[146:147], v[38:39]
	global_store_dwordx4 v56, v[144:147], s[10:11] offset:320
	v_pk_mul_f32 v[224:225], v[52:53], v[144:145]
	v_pk_mul_f32 v[226:227], v[54:55], v[146:147]
	v_cvt_pk_bf16_f32 v228, v224, v225
	v_cvt_pk_bf16_f32 v229, v226, v227
	global_store_dwordx2 v60, v[228:229], s[28:29] offset:160
	v_pk_mul_f32 v[230:231], v[144:145], v[144:145]
	v_pk_mul_f32 v[232:233], v[146:147], v[146:147]
	v_add_f32_e32 v230, v230, v231
	v_add_f32_e32 v230, v232, v230
	v_add_f32_e32 v230, v233, v230
	v_add_f32_e32 v235, v235, v230
	s_waitcnt vmcnt(29)
	v_pk_add_f32 v[68:69], v[68:69], v[40:41]
	v_pk_add_f32 v[70:71], v[70:71], v[42:43]
	global_store_dwordx4 v57, v[68:71], s[10:11]
	v_pk_mul_f32 v[224:225], v[240:241], v[68:69]
	v_pk_mul_f32 v[226:227], v[242:243], v[70:71]
	v_cvt_pk_bf16_f32 v228, v224, v225
	v_cvt_pk_bf16_f32 v229, v226, v227
	global_store_dwordx2 v61, v[228:229], s[28:29]
	v_pk_mul_f32 v[230:231], v[68:69], v[68:69]
	v_pk_mul_f32 v[232:233], v[70:71], v[70:71]
	v_add_f32_e32 v230, v230, v231
	v_add_f32_e32 v230, v232, v230
	v_add_f32_e32 v236, v233, v230
	s_waitcnt vmcnt(30)
	v_pk_add_f32 v[84:85], v[84:85], v[44:45]
	v_pk_add_f32 v[86:87], v[86:87], v[46:47]
	global_store_dwordx4 v57, v[84:87], s[10:11] offset:64
	v_pk_mul_f32 v[224:225], v[244:245], v[84:85]
	v_pk_mul_f32 v[226:227], v[246:247], v[86:87]
	v_cvt_pk_bf16_f32 v228, v224, v225
	v_cvt_pk_bf16_f32 v229, v226, v227
	global_store_dwordx2 v61, v[228:229], s[28:29] offset:32
	v_pk_mul_f32 v[230:231], v[84:85], v[84:85]
	v_pk_mul_f32 v[232:233], v[86:87], v[86:87]
	v_add_f32_e32 v230, v230, v231
	v_add_f32_e32 v230, v232, v230
	v_add_f32_e32 v230, v233, v230
	v_add_f32_e32 v236, v236, v230
	s_waitcnt vmcnt(31)
	v_pk_add_f32 v[100:101], v[100:101], v[160:161]
	v_pk_add_f32 v[102:103], v[102:103], v[162:163]
	global_store_dwordx4 v57, v[100:103], s[10:11] offset:128
	v_pk_mul_f32 v[224:225], v[248:249], v[100:101]
	v_pk_mul_f32 v[226:227], v[250:251], v[102:103]
	v_cvt_pk_bf16_f32 v228, v224, v225
	v_cvt_pk_bf16_f32 v229, v226, v227
	global_store_dwordx2 v61, v[228:229], s[28:29] offset:64
	v_pk_mul_f32 v[230:231], v[100:101], v[100:101]
	v_pk_mul_f32 v[232:233], v[102:103], v[102:103]
	v_add_f32_e32 v230, v230, v231
	v_add_f32_e32 v230, v232, v230
	v_add_f32_e32 v230, v233, v230
	v_add_f32_e32 v236, v236, v230
	s_waitcnt vmcnt(32)
	v_pk_add_f32 v[116:117], v[116:117], v[164:165]
	v_pk_add_f32 v[118:119], v[118:119], v[166:167]
	global_store_dwordx4 v57, v[116:119], s[10:11] offset:192
	v_pk_mul_f32 v[224:225], v[252:253], v[116:117]
	v_pk_mul_f32 v[226:227], v[254:255], v[118:119]
	v_cvt_pk_bf16_f32 v228, v224, v225
	v_cvt_pk_bf16_f32 v229, v226, v227
	global_store_dwordx2 v61, v[228:229], s[28:29] offset:96
	v_pk_mul_f32 v[230:231], v[116:117], v[116:117]
	v_pk_mul_f32 v[232:233], v[118:119], v[118:119]
	v_add_f32_e32 v230, v230, v231
	v_add_f32_e32 v230, v232, v230
	v_add_f32_e32 v237, v233, v230
	s_waitcnt vmcnt(33)
	v_pk_add_f32 v[132:133], v[132:133], v[168:169]
	v_pk_add_f32 v[134:135], v[134:135], v[170:171]
	global_store_dwordx4 v57, v[132:135], s[10:11] offset:256
	v_pk_mul_f32 v[224:225], v[48:49], v[132:133]
	v_pk_mul_f32 v[226:227], v[50:51], v[134:135]
	v_cvt_pk_bf16_f32 v228, v224, v225
	v_cvt_pk_bf16_f32 v229, v226, v227
	global_store_dwordx2 v61, v[228:229], s[28:29] offset:128
	v_pk_mul_f32 v[230:231], v[132:133], v[132:133]
	v_pk_mul_f32 v[232:233], v[134:135], v[134:135]
	v_add_f32_e32 v230, v230, v231
	v_add_f32_e32 v230, v232, v230
	v_add_f32_e32 v230, v233, v230
	v_add_f32_e32 v237, v237, v230
	s_waitcnt vmcnt(34)
	v_pk_add_f32 v[148:149], v[148:149], v[172:173]
	v_pk_add_f32 v[150:151], v[150:151], v[174:175]
	global_store_dwordx4 v57, v[148:151], s[10:11] offset:320
	v_pk_mul_f32 v[224:225], v[52:53], v[148:149]
	v_pk_mul_f32 v[226:227], v[54:55], v[150:151]
	v_cvt_pk_bf16_f32 v228, v224, v225
	v_cvt_pk_bf16_f32 v229, v226, v227
	global_store_dwordx2 v61, v[228:229], s[28:29] offset:160
	v_pk_mul_f32 v[230:231], v[148:149], v[148:149]
	v_pk_mul_f32 v[232:233], v[150:151], v[150:151]
	v_add_f32_e32 v230, v230, v231
	v_add_f32_e32 v230, v232, v230
	v_add_f32_e32 v230, v233, v230
	v_add_f32_e32 v237, v237, v230
	s_waitcnt vmcnt(35)
	v_pk_add_f32 v[72:73], v[72:73], v[176:177]
	v_pk_add_f32 v[74:75], v[74:75], v[178:179]
	global_store_dwordx4 v58, v[72:75], s[10:11]
	v_pk_mul_f32 v[224:225], v[240:241], v[72:73]
	v_pk_mul_f32 v[226:227], v[242:243], v[74:75]
	v_cvt_pk_bf16_f32 v228, v224, v225
	v_cvt_pk_bf16_f32 v229, v226, v227
	global_store_dwordx2 v62, v[228:229], s[28:29]
	v_pk_mul_f32 v[230:231], v[72:73], v[72:73]
	v_pk_mul_f32 v[232:233], v[74:75], v[74:75]
	v_add_f32_e32 v230, v230, v231
	v_add_f32_e32 v230, v232, v230
	v_add_f32_e32 v238, v233, v230
	s_waitcnt vmcnt(36)
	v_pk_add_f32 v[88:89], v[88:89], v[180:181]
	v_pk_add_f32 v[90:91], v[90:91], v[182:183]
	global_store_dwordx4 v58, v[88:91], s[10:11] offset:64
	v_pk_mul_f32 v[224:225], v[244:245], v[88:89]
	v_pk_mul_f32 v[226:227], v[246:247], v[90:91]
	v_cvt_pk_bf16_f32 v228, v224, v225
	v_cvt_pk_bf16_f32 v229, v226, v227
	global_store_dwordx2 v62, v[228:229], s[28:29] offset:32
	v_pk_mul_f32 v[230:231], v[88:89], v[88:89]
	v_pk_mul_f32 v[232:233], v[90:91], v[90:91]
	v_add_f32_e32 v230, v230, v231
	v_add_f32_e32 v230, v232, v230
	v_add_f32_e32 v230, v233, v230
	v_add_f32_e32 v238, v238, v230
	s_waitcnt vmcnt(37)
	v_pk_add_f32 v[104:105], v[104:105], v[184:185]
	v_pk_add_f32 v[106:107], v[106:107], v[186:187]
	global_store_dwordx4 v58, v[104:107], s[10:11] offset:128
	v_pk_mul_f32 v[224:225], v[248:249], v[104:105]
	v_pk_mul_f32 v[226:227], v[250:251], v[106:107]
	v_cvt_pk_bf16_f32 v228, v224, v225
	v_cvt_pk_bf16_f32 v229, v226, v227
	global_store_dwordx2 v62, v[228:229], s[28:29] offset:64
	v_pk_mul_f32 v[230:231], v[104:105], v[104:105]
	v_pk_mul_f32 v[232:233], v[106:107], v[106:107]
	v_add_f32_e32 v230, v230, v231
	v_add_f32_e32 v230, v232, v230
	v_add_f32_e32 v230, v233, v230
	v_add_f32_e32 v238, v238, v230
	s_waitcnt vmcnt(38)
	v_pk_add_f32 v[120:121], v[120:121], v[188:189]
	v_pk_add_f32 v[122:123], v[122:123], v[190:191]
	global_store_dwordx4 v58, v[120:123], s[10:11] offset:192
	v_pk_mul_f32 v[224:225], v[252:253], v[120:121]
	v_pk_mul_f32 v[226:227], v[254:255], v[122:123]
	v_cvt_pk_bf16_f32 v228, v224, v225
	v_cvt_pk_bf16_f32 v229, v226, v227
	global_store_dwordx2 v62, v[228:229], s[28:29] offset:96
	v_pk_mul_f32 v[230:231], v[120:121], v[120:121]
	v_pk_mul_f32 v[232:233], v[122:123], v[122:123]
	v_add_f32_e32 v230, v230, v231
	v_add_f32_e32 v230, v232, v230
	v_add_f32_e32 v239, v233, v230
	s_waitcnt vmcnt(39)
	v_pk_add_f32 v[136:137], v[136:137], v[192:193]
	v_pk_add_f32 v[138:139], v[138:139], v[194:195]
	global_store_dwordx4 v58, v[136:139], s[10:11] offset:256
	v_pk_mul_f32 v[224:225], v[48:49], v[136:137]
	v_pk_mul_f32 v[226:227], v[50:51], v[138:139]
	v_cvt_pk_bf16_f32 v228, v224, v225
	v_cvt_pk_bf16_f32 v229, v226, v227
	global_store_dwordx2 v62, v[228:229], s[28:29] offset:128
	v_pk_mul_f32 v[230:231], v[136:137], v[136:137]
	v_pk_mul_f32 v[232:233], v[138:139], v[138:139]
	v_add_f32_e32 v230, v230, v231
	v_add_f32_e32 v230, v232, v230
	v_add_f32_e32 v230, v233, v230
	v_add_f32_e32 v239, v239, v230
	s_waitcnt vmcnt(40)
	v_pk_add_f32 v[152:153], v[152:153], v[196:197]
	v_pk_add_f32 v[154:155], v[154:155], v[198:199]
	global_store_dwordx4 v58, v[152:155], s[10:11] offset:320
	v_pk_mul_f32 v[224:225], v[52:53], v[152:153]
	v_pk_mul_f32 v[226:227], v[54:55], v[154:155]
	v_cvt_pk_bf16_f32 v228, v224, v225
	v_cvt_pk_bf16_f32 v229, v226, v227
	global_store_dwordx2 v62, v[228:229], s[28:29] offset:160
	v_pk_mul_f32 v[230:231], v[152:153], v[152:153]
	v_pk_mul_f32 v[232:233], v[154:155], v[154:155]
	v_add_f32_e32 v230, v230, v231
	v_add_f32_e32 v230, v232, v230
	v_add_f32_e32 v230, v233, v230
	v_add_f32_e32 v239, v239, v230
	s_waitcnt vmcnt(41)
	v_pk_add_f32 v[76:77], v[76:77], v[200:201]
	v_pk_add_f32 v[78:79], v[78:79], v[202:203]
	global_store_dwordx4 v59, v[76:79], s[10:11]
	v_pk_mul_f32 v[224:225], v[240:241], v[76:77]
	v_pk_mul_f32 v[226:227], v[242:243], v[78:79]
	v_cvt_pk_bf16_f32 v228, v224, v225
	v_cvt_pk_bf16_f32 v229, v226, v227
	global_store_dwordx2 v63, v[228:229], s[28:29]
	v_pk_mul_f32 v[230:231], v[76:77], v[76:77]
	v_pk_mul_f32 v[232:233], v[78:79], v[78:79]
	v_add_f32_e32 v230, v230, v231
	v_add_f32_e32 v230, v232, v230
	v_add_f32_e32 v14, v233, v230
	s_waitcnt vmcnt(42)
	v_pk_add_f32 v[92:93], v[92:93], v[204:205]
	v_pk_add_f32 v[94:95], v[94:95], v[206:207]
	global_store_dwordx4 v59, v[92:95], s[10:11] offset:64
	v_pk_mul_f32 v[224:225], v[244:245], v[92:93]
	v_pk_mul_f32 v[226:227], v[246:247], v[94:95]
	v_cvt_pk_bf16_f32 v228, v224, v225
	v_cvt_pk_bf16_f32 v229, v226, v227
	global_store_dwordx2 v63, v[228:229], s[28:29] offset:32
	v_pk_mul_f32 v[230:231], v[92:93], v[92:93]
	v_pk_mul_f32 v[232:233], v[94:95], v[94:95]
	v_add_f32_e32 v230, v230, v231
	v_add_f32_e32 v230, v232, v230
	v_add_f32_e32 v230, v233, v230
	v_add_f32_e32 v14, v14, v230
	s_waitcnt vmcnt(43)
	v_pk_add_f32 v[108:109], v[108:109], v[208:209]
	v_pk_add_f32 v[110:111], v[110:111], v[210:211]
	global_store_dwordx4 v59, v[108:111], s[10:11] offset:128
	v_pk_mul_f32 v[224:225], v[248:249], v[108:109]
	v_pk_mul_f32 v[226:227], v[250:251], v[110:111]
	v_cvt_pk_bf16_f32 v228, v224, v225
	v_cvt_pk_bf16_f32 v229, v226, v227
	global_store_dwordx2 v63, v[228:229], s[28:29] offset:64
	v_pk_mul_f32 v[230:231], v[108:109], v[108:109]
	v_pk_mul_f32 v[232:233], v[110:111], v[110:111]
	v_add_f32_e32 v230, v230, v231
	v_add_f32_e32 v230, v232, v230
	v_add_f32_e32 v230, v233, v230
	v_add_f32_e32 v14, v14, v230
	s_waitcnt vmcnt(44)
	v_pk_add_f32 v[124:125], v[124:125], v[212:213]
	v_pk_add_f32 v[126:127], v[126:127], v[214:215]
	global_store_dwordx4 v59, v[124:127], s[10:11] offset:192
	v_pk_mul_f32 v[224:225], v[252:253], v[124:125]
	v_pk_mul_f32 v[226:227], v[254:255], v[126:127]
	v_cvt_pk_bf16_f32 v228, v224, v225
	v_cvt_pk_bf16_f32 v229, v226, v227
	global_store_dwordx2 v63, v[228:229], s[28:29] offset:96
	v_pk_mul_f32 v[230:231], v[124:125], v[124:125]
	v_pk_mul_f32 v[232:233], v[126:127], v[126:127]
	v_add_f32_e32 v230, v230, v231
	v_add_f32_e32 v230, v232, v230
	v_add_f32_e32 v15, v233, v230
	s_waitcnt vmcnt(45)
	v_pk_add_f32 v[140:141], v[140:141], v[216:217]
	v_pk_add_f32 v[142:143], v[142:143], v[218:219]
	global_store_dwordx4 v59, v[140:143], s[10:11] offset:256
	v_pk_mul_f32 v[224:225], v[48:49], v[140:141]
	v_pk_mul_f32 v[226:227], v[50:51], v[142:143]
	v_cvt_pk_bf16_f32 v228, v224, v225
	v_cvt_pk_bf16_f32 v229, v226, v227
	global_store_dwordx2 v63, v[228:229], s[28:29] offset:128
	v_pk_mul_f32 v[230:231], v[140:141], v[140:141]
	v_pk_mul_f32 v[232:233], v[142:143], v[142:143]
	v_add_f32_e32 v230, v230, v231
	v_add_f32_e32 v230, v232, v230
	v_add_f32_e32 v230, v233, v230
	v_add_f32_e32 v15, v15, v230
	s_waitcnt vmcnt(46)
	v_pk_add_f32 v[156:157], v[156:157], v[220:221]
	v_pk_add_f32 v[158:159], v[158:159], v[222:223]
	global_store_dwordx4 v59, v[156:159], s[10:11] offset:320
	v_pk_mul_f32 v[224:225], v[52:53], v[156:157]
	v_pk_mul_f32 v[226:227], v[54:55], v[158:159]
	v_cvt_pk_bf16_f32 v228, v224, v225
	v_cvt_pk_bf16_f32 v229, v226, v227
	global_store_dwordx2 v63, v[228:229], s[28:29] offset:160
	v_pk_mul_f32 v[230:231], v[156:157], v[156:157]
	v_pk_mul_f32 v[232:233], v[158:159], v[158:159]
	v_add_f32_e32 v230, v230, v231
	v_add_f32_e32 v230, v232, v230
	v_add_f32_e32 v230, v233, v230
	v_add_f32_e32 v15, v15, v230
	ds_bpermute_b32 v224, v13, v234
	ds_bpermute_b32 v225, v13, v235
	ds_bpermute_b32 v226, v13, v236
	ds_bpermute_b32 v227, v13, v237
	ds_bpermute_b32 v228, v13, v238
	ds_bpermute_b32 v229, v13, v239
	ds_bpermute_b32 v230, v13, v14
	ds_bpermute_b32 v231, v13, v15
	s_waitcnt lgkmcnt(0)
	v_add_f32_e32 v234, v234, v224
	v_add_f32_e32 v235, v235, v225
	v_add_f32_e32 v236, v236, v226
	v_add_f32_e32 v237, v237, v227
	v_add_f32_e32 v238, v238, v228
	v_add_f32_e32 v239, v239, v229
	v_add_f32_e32 v14, v14, v230
	v_add_f32_e32 v15, v15, v231
	ds_bpermute_b32 v224, v12, v234
	ds_bpermute_b32 v225, v12, v235
	ds_bpermute_b32 v226, v12, v236
	ds_bpermute_b32 v227, v12, v237
	ds_bpermute_b32 v228, v12, v238
	ds_bpermute_b32 v229, v12, v239
	ds_bpermute_b32 v230, v12, v14
	ds_bpermute_b32 v231, v12, v15
	s_waitcnt lgkmcnt(0)
	v_add_f32_e32 v234, v234, v224
	v_add_f32_e32 v235, v235, v225
	v_add_f32_e32 v236, v236, v226
	v_add_f32_e32 v237, v237, v227
	v_add_f32_e32 v238, v238, v228
	v_add_f32_e32 v239, v239, v229
	v_add_f32_e32 v14, v14, v230
	v_add_f32_e32 v15, v15, v231
	s_and_saveexec_b64 s[2:3], vcc
	global_store_dwordx2 v8, v[234:235], s[26:27]
	global_store_dwordx2 v9, v[236:237], s[26:27]
	global_store_dwordx2 v10, v[238:239], s[26:27]
	global_store_dwordx2 v11, v[14:15], s[26:27]
	s_or_b64 exec, exec, s[2:3]
